# FoX unit prologue: pruning loads of both heads issued in one batch behind the Q loads
# baseline (speedup 1.0000x reference)
.LBB0_479:
	s_or_b64 exec, exec, s[2:3]
	s_waitcnt lgkmcnt(0)
	s_barrier
	ds_read_b32 v1, v205
	s_mov_b64 s[2:3], -1
	s_waitcnt lgkmcnt(0)
	v_cmp_le_i32_e32 vcc, s29, v1
	v_readfirstlane_b32 s4, v1
	s_cbranch_vccnz .LBB0_474
	s_add_i32 s2, s4, 0xfffffe00
	s_cmpk_gt_i32 s4, 0x1ff
	s_cselect_b32 s2, s2, s4
	s_ashr_i32 s3, s2, 31
	s_lshr_b32 s3, s3, 26
	s_add_i32 s3, s2, s3
	s_ashr_i32 s52, s3, 6
	s_andn2_b32 s3, s3, 63
	s_sub_i32 s2, s2, s3
	v_mov_b32_e32 v1, v0
	s_ashr_i32 s20, s2, 2
	s_lshl_b32 s2, s2, 1
	v_readfirstlane_b32 s56, v1
	s_ashr_i32 s50, s56, 6
	s_ashr_i32 s51, s56, 8
	s_and_b32 s55, s2, 6
	s_sub_i32 s54, 7, s52
	s_and_b32 s53, s50, 3
	s_add_i32 s3, s51, s55
	s_ashr_i32 s21, s20, 31
	s_lshl_b32 s2, s54, 8
	s_lshl_b32 s57, s53, 6
	s_lshl_b32 s18, s3, 6
	s_or_b32 s6, s57, s2
	s_lshl_b64 s[4:5], s[20:21], 20
	s_ashr_i32 s19, s18, 31
	s_add_u32 s4, s4, s18
	v_and_b32_e32 v230, 31, v1
	s_addc_u32 s5, s5, s19
	v_or_b32_e32 v2, s6, v230
	s_lshl_b64 s[22:23], s[4:5], 1
	v_or_b32_e32 v4, 32, v2
	s_add_u32 s4, s30, s22
	v_mov_b32_e32 v5, v3
	s_addc_u32 s5, s31, s23
	v_lshlrev_b64 v[6:7], 10, v[2:3]
	v_lshlrev_b64 v[4:5], 10, v[4:5]
	s_lshl_b32 s58, s20, 3
	v_lshl_add_u64 v[6:7], s[4:5], 0, v[6:7]
	v_lshl_add_u64 v[4:5], s[4:5], 0, v[4:5]
	s_add_i32 s4, s3, s58
	s_ashr_i32 s5, s4, 31
	v_bfe_u32 v229, v1, 5, 1
	s_lshl_b64 s[4:5], s[4:5], 13
	v_lshlrev_b32_e32 v8, 4, v229
	v_mov_b32_e32 v9, v3
	s_add_u32 s4, s33, s4
	v_lshl_add_u64 v[4:5], v[4:5], 0, v[8:9]
	s_addc_u32 s5, s34, s5
	v_lshl_add_u64 v[6:7], v[6:7], 0, v[8:9]
	v_lshl_add_u64 v[8:9], v[2:3], 2, s[4:5]
	global_load_dwordx4 v[162:165], v[4:5], off offset:96
	global_load_dwordx4 v[166:169], v[4:5], off offset:64
	global_load_dwordx4 v[170:173], v[6:7], off offset:96
	global_load_dwordx4 v[174:177], v[6:7], off offset:64
	global_load_dwordx4 v[178:181], v[4:5], off offset:32
	global_load_dwordx4 v[182:185], v[4:5], off
	global_load_dwordx4 v[186:189], v[6:7], off offset:32
	global_load_dwordx4 v[190:193], v[6:7], off
	global_load_dword v232, v[8:9], off offset:128
	global_load_dword v233, v[8:9], off
	s_or_b32 s24, s55, s58
	s_ashr_i32 s25, s24, 31
	s_add_i32 s59, s58, 0x80
	s_lshl_b64 s[26:27], s[24:25], 13
	s_add_u32 s26, s33, s26
	s_addc_u32 s27, s34, s27
	s_lshl_b64 s[60:61], s[24:25], 2
	s_add_u32 s60, s35, s60
	s_mov_b32 s5, s7
	s_addc_u32 s61, s38, s61
	s_or_b32 s4, s59, s55
	v_mov_b32_e32 v2, v3
	v_mov_b32_e32 v4, v3
	s_lshl_b64 s[4:5], s[4:5], 2
	s_add_u32 s4, s35, s4
	s_addc_u32 s5, s38, s5
	s_mov_b32 s3, s7
	v_lshlrev_b32_e32 v5, 8, v230
	v_mov_b32_e32 v234, 0
	global_load_dword v2, v3, s[60:61]
	global_load_dword v4, v3, s[4:5]
	s_lshl_b64 s[4:5], s[2:3], 2
	s_add_u32 s2, s26, s4
	s_addc_u32 s3, s27, s5
	v_mov_b32_e32 v118, 0x2000
	v_add_u32_e32 v119, 0x2000, v5
	global_load_dword v6, v3, s[2:3]
	s_nop 0
	global_load_dword v5, v5, s[26:27] offset:252
	s_lshl_b64 s[98:99], s[6:7], 2
	s_add_u32 s98, s26, s98
	s_addc_u32 s99, s27, s99
	global_load_dword v114, v3, s[60:61] offset:4
	global_load_dword v115, v3, s[60:61] offset:516
	global_load_dword v116, v118, s[2:3]
	global_load_dword v117, v119, s[26:27] offset:252
	global_load_dword v120, v3, s[98:99]
	global_load_dword v121, v118, s[98:99]
	s_cmpk_gt_u32 s56, 0xff
	s_waitcnt vmcnt(2)
	v_mul_f32_e32 v2, v2, v4
	v_mul_f32_e32 v4, 0x4f800000, v2
	v_cmp_gt_f32_e32 vcc, s44, v2
	s_waitcnt vmcnt(0)
	v_sub_f32_e32 v5, v6, v5
	v_cndmask_b32_e32 v2, v2, v4, vcc
	v_sqrt_f32_e32 v4, v2
	s_nop 0
	v_add_u32_e32 v6, -1, v4
	v_add_u32_e32 v7, 1, v4
	v_fma_f32 v8, -v6, v4, v2
	v_fma_f32 v9, -v7, v4, v2
	v_cmp_ge_f32_e64 s[2:3], 0, v8
	s_nop 1
	v_cndmask_b32_e64 v4, v4, v6, s[2:3]
	v_cmp_lt_f32_e64 s[2:3], 0, v9
	s_nop 1
	v_cndmask_b32_e64 v4, v4, v7, s[2:3]
	v_mul_f32_e32 v6, 0x37800000, v4
	v_cndmask_b32_e32 v4, v4, v6, vcc
	v_cmp_class_f32_e32 vcc, v2, v226
	s_nop 1
	v_cndmask_b32_e32 v2, v4, v2, vcc
	v_fmac_f32_e32 v5, 2.0, v2
	v_cmp_le_f32_e32 vcc, s45, v5
	s_cbranch_scc1 .LBB0_482
	s_lshl_b64 s[2:3], s[6:7], 2
	s_add_u32 s2, s26, s2
	s_addc_u32 s3, s27, s3
	v_mov_b32_e32 v4, v120
	v_add_f32_e32 v2, v2, v2
	v_add_f32_e32 v2, 0x42480000, v2
	s_waitcnt vmcnt(0)
	v_add_f32_e32 v234, v2, v4
.LBB0_482:
	s_or_b32 s25, s55, 1
	s_or_b32 s2, s25, s58
	s_ashr_i32 s3, s2, 31
	s_lshl_b64 s[26:27], s[2:3], 13
	s_add_u32 s26, s33, s26
	s_addc_u32 s27, s34, s27
	s_lshl_b64 s[2:3], s[2:3], 2
	s_add_u32 s2, s35, s2
	s_addc_u32 s3, s38, s3
	s_or_b32 s58, s25, s59
	s_mov_b32 s59, s7
	s_lshl_b64 s[58:59], s[58:59], 2
	s_add_u32 s58, s35, s58
	s_addc_u32 s59, s38, s59
	v_mov_b32_e32 v2, v114
	v_mov_b32_e32 v4, v115
	v_lshlrev_b32_e32 v5, 6, v230
	s_add_u32 s2, s26, s4
	s_addc_u32 s3, s27, s5
	v_lshlrev_b32_e32 v5, 2, v5
	v_mov_b32_e32 v6, v116
	s_nop 0
	v_mov_b32_e32 v5, v117
	s_cmp_lg_u32 s51, 1
	s_waitcnt vmcnt(2)
	v_mul_f32_e32 v2, v2, v4
	v_mul_f32_e32 v4, 0x4f800000, v2
	v_cmp_gt_f32_e64 s[2:3], s44, v2
	s_waitcnt vmcnt(0)
	v_sub_f32_e32 v5, v6, v5
	v_cndmask_b32_e64 v2, v2, v4, s[2:3]
	v_sqrt_f32_e32 v4, v2
	s_nop 0
	v_add_u32_e32 v6, -1, v4
	v_add_u32_e32 v7, 1, v4
	v_fma_f32 v8, -v6, v4, v2
	v_fma_f32 v9, -v7, v4, v2
	v_cmp_ge_f32_e64 s[4:5], 0, v8
	s_nop 1
	v_cndmask_b32_e64 v4, v4, v6, s[4:5]
	v_cmp_lt_f32_e64 s[4:5], 0, v9
	s_nop 1
	v_cndmask_b32_e64 v4, v4, v7, s[4:5]
	v_mul_f32_e32 v6, 0x37800000, v4
	v_cndmask_b32_e64 v4, v4, v6, s[2:3]
	v_cmp_class_f32_e64 s[2:3], v2, v226
	s_nop 1
	v_cndmask_b32_e64 v2, v4, v2, s[2:3]
	v_fmac_f32_e32 v5, 2.0, v2
	v_cmp_le_f32_e64 s[2:3], s45, v5
	s_cbranch_scc1 .LBB0_484
	s_lshl_b64 s[4:5], s[6:7], 2
	s_add_u32 s4, s26, s4
	s_addc_u32 s5, s27, s5
	v_mov_b32_e32 v4, v121
	v_add_f32_e32 v2, v2, v2
	v_add_f32_e32 v2, 0x42480000, v2
	s_waitcnt vmcnt(0)
	v_add_f32_e32 v234, v2, v4
